# mLSTM: row-sum reduction by DPP adds instead of three LDS permute round trips; wave 0 issues its per-chunk table reads at the top of the chunk
# speedup vs baseline: 1.0031x; 1.0031x over previous
.LBB0_726:
	v_mov_b32_e32 v3, v148
	v_mov_b32_e32 v2, v149
	s_andn2_b64 vcc, exec, s[40:41]
	s_cbranch_vccnz .Lml_w0_early_done
	v_add_u32_e32 v72, s90, v110
	v_mov_b32_e32 v79, s20
	v_add_u32_e32 v73, 0xffffbf04, v72
	v_add_u32_e32 v74, 0xffffdf04, v72
	v_add_u32_e32 v72, 0xffffff04, v72
	v_mov_b32_e32 v78, s90
	ds_read_b32 v79, v79
	ds_read_b32 v73, v73
	ds_read_b32 v72, v72
	ds_read_b32 v74, v74
	ds_read_b32 v78, v78
.Lml_w0_early_done:
	s_waitcnt vmcnt(8)
	ds_write_b128 v99, v[4:7]
	ds_write_b128 v99, v[8:11] offset:33792
	ds_write_b128 v139, v[12:15]
	ds_write_b128 v139, v[16:19] offset:33792
	ds_write_b128 v140, v[20:23]
	ds_write_b128 v140, v[24:27] offset:33792
	ds_write_b128 v141, v[28:31]
	ds_write_b128 v141, v[32:35] offset:33792
	s_cmp_eq_u32 s88, 0x3e0000
	s_cbranch_scc1 .Lml_no_qk_fetch
	s_add_u32 s80, s94, s88
	v_mov_b32_e32 v0, v117
	s_addc_u32 s81, s18, s89
	s_nop 0
	v_lshl_add_u64 v[28:29], s[80:81], 0, v[0:1]
	v_add_co_u32_e32 v4, vcc, 0x2e820000, v28
	s_nop 1
	v_addc_co_u32_e32 v5, vcc, 0, v29, vcc
	v_add_co_u32_e32 v8, vcc, 0x32820000, v28
	s_nop 1
	v_addc_co_u32_e32 v9, vcc, 0, v29, vcc
	v_add_co_u32_e32 v12, vcc, 0x2e828000, v28
	global_load_dwordx4 v[4:7], v[4:5], off
	s_nop 0
	global_load_dwordx4 v[8:11], v[8:9], off
	v_addc_co_u32_e32 v13, vcc, 0, v29, vcc
	v_add_co_u32_e32 v16, vcc, 0x32828000, v28
	s_nop 1
	v_addc_co_u32_e32 v17, vcc, 0, v29, vcc
	v_add_co_u32_e32 v20, vcc, 0x2e830000, v28
	global_load_dwordx4 v[12:15], v[12:13], off
	s_nop 0
	global_load_dwordx4 v[16:19], v[16:17], off
	v_addc_co_u32_e32 v21, vcc, 0, v29, vcc
	v_add_co_u32_e32 v24, vcc, 0x32830000, v28
	s_nop 1
	v_addc_co_u32_e32 v25, vcc, 0, v29, vcc
	v_add_co_u32_e32 v30, vcc, 0x2e838000, v28
	global_load_dwordx4 v[20:23], v[20:21], off
	s_nop 0
	global_load_dwordx4 v[24:27], v[24:25], off
	v_addc_co_u32_e32 v31, vcc, 0, v29, vcc
	v_add_co_u32_e32 v32, vcc, 0x32838000, v28
	s_nop 1
	v_addc_co_u32_e32 v33, vcc, 0, v29, vcc
	global_load_dwordx4 v[28:31], v[30:31], off
	s_nop 0
	global_load_dwordx4 v[32:35], v[32:33], off
	s_nop 0
.Lml_no_qk_fetch:
	s_andn2_b64 vcc, exec, s[40:41]
	s_cbranch_vccnz .LBB0_730
	s_waitcnt lgkmcnt(8)
	v_max_f32_e32 v75, v79, v79
	v_max_f32_e32 v72, v72, v72
	v_max_f32_e32 v76, v75, v72
	v_mul_f32_e32 v77, 0x3fb8aa3b, v76
	v_add_f32_e32 v74, v74, v76
	v_mul_f32_e32 v74, 0xbfb8aa3b, v74
	v_exp_f32_e32 v74, v74
	v_max_f32_e32 v72, v78, v78
	v_max_f32_e32 v72, v75, v72
	v_mul_f32_e32 v75, 0x3fb8aa3b, v73
	ds_write2st64_b32 v123, v75, v77 offset1:1
	v_sub_f32_e32 v75, v79, v76
	v_sub_f32_e32 v73, v73, v72
	v_mul_f32_e32 v75, 0x3fb8aa3b, v75
	v_mul_f32_e32 v73, 0x3fb8aa3b, v73
	v_exp_f32_e32 v75, v75
	v_exp_f32_e32 v73, v73
	ds_write2st64_b32 v123, v75, v74 offset0:2 offset1:3
	ds_write_b32 v123, v73 offset:1024
	s_and_saveexec_b64 s[80:81], s[44:45]
	s_cbranch_execz .LBB0_729
	v_sub_f32_e32 v0, v79, v72
	v_mul_f32_e32 v0, 0x3fb8aa3b, v0
	v_exp_f32_e32 v0, v0
	v_mov_b32_e32 v72, s19
	ds_write_b32 v72, v0

.LBB0_732:
	ds_read_b128 v[92:95], v166
	v_add_u32_e32 v167, 0, v3
	v_add_u32_e32 v0, 0x10800, v167
	v_add_u32_e32 v3, 0x10a40, v167
	ds_read_b64_tr_b16 v[72:73], v0
	ds_read_b64_tr_b16 v[74:75], v3
	ds_read_b128 v[168:171], v166 offset:64
	v_add_u32_e32 v0, 0x11a00, v167
	v_add_u32_e32 v174, 0x11c40, v167
	ds_read_b32 v3, v124 offset:512
	ds_read_b64_tr_b16 v[172:173], v0
	ds_read_b64_tr_b16 v[174:175], v174
	ds_read_b128 v[176:179], v166 offset:2304
	ds_read_b128 v[180:183], v145
	s_waitcnt lgkmcnt(6)
	v_mfma_f32_16x16x32_bf16 v[92:95], v[92:95], v[72:75], 0
	s_waitcnt lgkmcnt(0)
	v_lshlrev_b32_e32 v0, 16, v180
	v_mfma_f32_16x16x32_bf16 v[92:95], v[168:171], v[172:175], v[92:95]
	ds_read_b128 v[168:171], v145 offset:16
	ds_read_b128 v[184:187], v145 offset:32
	ds_read_b128 v[188:191], v145 offset:48
	ds_read_b128 v[194:197], v146
	ds_read_b128 v[198:201], v146 offset:16
	ds_read_b128 v[202:205], v146 offset:32
	ds_read_b128 v[206:209], v146 offset:48
	v_and_b32_e32 v180, 0xffff0000, v180
	s_waitcnt lgkmcnt(3)
	v_mul_f32_e32 v180, v195, v180
	v_fmac_f32_e32 v180, v194, v0
	v_lshlrev_b32_e32 v0, 16, v181
	v_and_b32_e32 v181, 0xffff0000, v181
	v_mul_f32_e32 v181, v197, v181
	v_fmac_f32_e32 v181, v196, v0
	v_add_f32_e32 v0, v180, v181
	v_and_b32_e32 v181, 0xffff0000, v182
	v_lshlrev_b32_e32 v180, 16, v182
	s_waitcnt lgkmcnt(2)
	v_mul_f32_e32 v181, v199, v181
	v_fmac_f32_e32 v181, v198, v180
	v_add_f32_e32 v0, v181, v0
	v_and_b32_e32 v181, 0xffff0000, v183
	v_lshlrev_b32_e32 v180, 16, v183
	v_mul_f32_e32 v181, v201, v181
	v_fmac_f32_e32 v181, v200, v180
	v_lshlrev_b32_e32 v180, 16, v168
	v_and_b32_e32 v168, 0xffff0000, v168
	s_waitcnt lgkmcnt(1)
	v_mul_f32_e32 v168, v203, v168
	v_fmac_f32_e32 v168, v202, v180
	v_lshlrev_b32_e32 v180, 16, v169
	v_and_b32_e32 v169, 0xffff0000, v169
	v_mul_f32_e32 v169, v205, v169
	v_fmac_f32_e32 v169, v204, v180
	v_add_f32_e32 v168, v168, v169
	v_lshlrev_b32_e32 v169, 16, v170
	v_and_b32_e32 v170, 0xffff0000, v170
	s_waitcnt lgkmcnt(0)
	v_mul_f32_e32 v170, v207, v170
	v_fmac_f32_e32 v170, v206, v169
	v_add_f32_e32 v168, v170, v168
	v_and_b32_e32 v170, 0xffff0000, v171
	v_lshlrev_b32_e32 v169, 16, v171
	v_mul_f32_e32 v170, v209, v170
	v_fmac_f32_e32 v170, v208, v169
	v_add_f32_e32 v180, v170, v168
	ds_read_b128 v[168:171], v146 offset:64
	v_add_f32_e32 v0, v181, v0
	v_add_f32_e32 v0, 0, v0
	v_add_f32_e32 v0, v0, v180
	ds_read_b128 v[180:183], v146 offset:80
	v_lshlrev_b32_e32 v194, 16, v184
	v_and_b32_e32 v184, 0xffff0000, v184
	s_waitcnt lgkmcnt(1)
	v_mul_f32_e32 v169, v169, v184
	v_and_b32_e32 v184, 0xffff0000, v185
	v_fmac_f32_e32 v169, v168, v194
	v_lshlrev_b32_e32 v168, 16, v185
	v_mul_f32_e32 v171, v171, v184
	v_fmac_f32_e32 v171, v170, v168
	v_and_b32_e32 v170, 0xffff0000, v186
	v_add_f32_e32 v168, v169, v171
	v_lshlrev_b32_e32 v169, 16, v186
	s_waitcnt lgkmcnt(0)
	v_mul_f32_e32 v170, v181, v170
	v_fmac_f32_e32 v170, v180, v169
	v_add_f32_e32 v168, v170, v168
	v_and_b32_e32 v170, 0xffff0000, v187
	v_lshlrev_b32_e32 v169, 16, v187
	v_mul_f32_e32 v170, v183, v170
	v_fmac_f32_e32 v170, v182, v169
	v_add_f32_e32 v180, v170, v168
	ds_read_b128 v[168:171], v146 offset:96
	v_add_f32_e32 v0, v0, v180
	ds_read_b128 v[180:183], v146 offset:112
	v_and_b32_e32 v185, 0xffff0000, v188
	v_lshlrev_b32_e32 v184, 16, v188
	s_waitcnt lgkmcnt(1)
	v_mul_f32_e32 v169, v169, v185
	v_fmac_f32_e32 v169, v168, v184
	v_and_b32_e32 v184, 0xffff0000, v189
	v_lshlrev_b32_e32 v168, 16, v189
	v_mul_f32_e32 v171, v171, v184
	v_fmac_f32_e32 v171, v170, v168
	v_and_b32_e32 v170, 0xffff0000, v190
	v_add_f32_e32 v168, v169, v171
	v_lshlrev_b32_e32 v169, 16, v190
	s_waitcnt lgkmcnt(0)
	v_mul_f32_e32 v170, v181, v170
	v_fmac_f32_e32 v170, v180, v169
	v_add_f32_e32 v180, v170, v168
	ds_read_b128 v[168:171], v147
	v_and_b32_e32 v184, 0xffff0000, v191
	v_lshlrev_b32_e32 v181, 16, v191
	v_mul_f32_e32 v183, v183, v184
	v_fmac_f32_e32 v183, v182, v181
	v_add_f32_e32 v180, v183, v180
	v_add_f32_e32 v0, v0, v180
	s_waitcnt lgkmcnt(0)
	v_lshlrev_b32_e32 v180, 16, v168
	v_and_b32_e32 v168, 0xffff0000, v168
	v_add_f32_e32 v168, v180, v168
	v_lshlrev_b32_e32 v180, 16, v169
	v_and_b32_e32 v169, 0xffff0000, v169
	v_add_f32_e32 v169, v180, v169
	v_add_f32_e32 v168, v168, v169
	v_lshlrev_b32_e32 v169, 16, v170
	v_and_b32_e32 v170, 0xffff0000, v170
	v_add_f32_e32 v169, v169, v170
	v_add_f32_e32 v168, v169, v168
	v_lshlrev_b32_e32 v169, 16, v171
	v_and_b32_e32 v170, 0xffff0000, v171
	v_add_f32_e32 v169, v169, v170
	v_add_f32_e32 v180, v169, v168
	v_fmac_f32_e32 v180, v3, v0
	ds_read_b128 v[168:171], v166 offset:2368
	v_mfma_f32_16x16x32_bf16 v[72:75], v[176:179], v[72:75], 0
	s_nop 0
	v_add_f32_dpp v0, v180, v180 quad_perm:[1,0,3,2] row_mask:0xf bank_mask:0xf
	s_nop 1
	v_add_f32_dpp v3, v0, v0 quad_perm:[2,3,0,1] row_mask:0xf bank_mask:0xf
	s_nop 1
	v_add_f32_dpp v0, v3, v3 row_half_mirror row_mask:0xf bank_mask:0xf
	s_waitcnt lgkmcnt(0)
	v_mfma_f32_16x16x32_bf16 v[72:75], v[168:171], v[172:175], v[72:75]
	s_and_saveexec_b64 s[80:81], s[58:59]
	s_cbranch_execz .LBB0_734
	ds_write_b32 v124, v0 offset:1280
